# attention loops: ones fragment kept in free registers, blanket s_nop after inline v_max3 dropped; on top of router/epilogue/index-fill/silu/process-slot edits
# speedup vs baseline: 1.0084x; 1.0037x over previous
.LBB0_1579:
	v_lshlrev_b32_e32 v36, 5, v179
	v_and_b32_e32 v36, 0x180, v36
	v_lshlrev_b32_e32 v38, 3, v179
	v_lshl_or_b32 v36, v98, 9, v36
	v_lshlrev_b32_e32 v37, 5, v187
	v_and_b32_e32 v38, 24, v38
	v_or3_b32 v36, v36, v37, v38
	v_lshlrev_b32_e32 v37, 6, v186
	v_and_or_b32 v209, v37, 64, v36
	v_bitop3_b32 v210, v36, 64, v37 bitop3:0x34
	v_and_b32_e32 v37, 7, v179
	v_and_b32_e32 v36, 30, v188
	v_lshlrev_b32_e32 v229, 10, v37
	v_lshlrev_b32_e32 v37, 4, v37
	v_lshl_or_b32 v200, v36, 11, v37
	v_lshrrev_b32_e32 v36, 1, v179
	v_and_b32_e32 v228, 28, v36
	v_lshlrev_b32_e32 v36, 3, v185
	v_and_b32_e32 v37, 4, v179
	v_and_or_b32 v36, v36, 24, v37
	v_lshlrev_b32_e32 v198, 2, v36
	v_bitop3_b32 v36, v179, 5, 7 bitop3:0x6c
	v_bfe_u32 v39, v188, 2, 3
	v_lshlrev_b32_e32 v37, 3, v36
	v_bitop3_b32 v39, v39, v179, 7 bitop3:0x78
	v_bitop3_b32 v36, v37, 28, v36 bitop3:0xc8
	v_lshlrev_b32_e32 v230, 4, v39
	v_lshlrev_b32_e32 v39, 2, v188
	v_lshlrev_b32_e32 v188, 2, v36
	v_bitop3_b32 v36, v179, 6, 7 bitop3:0x6c
	v_lshlrev_b32_e32 v37, 3, v36
	v_bitop3_b32 v36, v37, 28, v36 bitop3:0xc8
	s_lshl_b32 s4, s76, 10
	v_lshlrev_b32_e32 v186, 2, v36
	v_bitop3_b32 v36, v179, 7, v179 bitop3:0xc
	s_waitcnt lgkmcnt(0)
	s_barrier
	s_sub_i32 s17, 0, s4
	v_lshlrev_b32_e32 v37, 3, v36
	s_add_i32 s4, 0, 0x8000
	s_lshl_b32 s15, s76, 4
	v_mov_b32_e32 v177, v99
	v_add_u32_e32 v38, 0, v229
	v_and_b32_e32 v231, 8, v39
	v_bitop3_b32 v36, v37, 28, v36 bitop3:0xc8
	v_add_u32_e32 v205, s4, v209
	v_add_u32_e32 v67, s4, v210
	s_add_i32 s4, 0, 0x6000
	v_lshlrev_b32_e32 v35, 3, v175
	s_lshl_b32 s12, s40, 6
	s_mov_b32 s14, 3
	s_add_i32 s16, s41, 0
	v_lshl_add_u64 v[202:203], s[56:57], 0, v[176:177]
	v_and_b32_e32 v232, -2, v189
	v_add3_u32 v233, v38, v230, v231
	v_mov_b32_e32 v201, v99
	s_lshl_b32 s13, s78, 1
	v_mov_b32_e32 v199, v99
	v_xor_b32_e32 v196, 32, v198
	v_mov_b32_e32 v197, v99
	v_xor_b32_e32 v194, 64, v198
	v_mov_b32_e32 v195, v99
	v_xor_b32_e32 v192, 0x60, v198
	v_mov_b32_e32 v193, v99
	v_xor_b32_e32 v190, 16, v198
	v_mov_b32_e32 v191, v99
	v_mov_b32_e32 v189, v99
	v_mov_b32_e32 v187, v99
	v_lshlrev_b32_e32 v64, 2, v36
	v_mov_b32_e32 v65, v99
	v_cmp_eq_u32_e64 s[34:35], 0, v185
	v_mov_b32_e32 v175, v99
	v_mov_b32_e32 v179, v99
	v_mov_b32_e32 v185, v99
	v_add_u32_e32 v234, s4, v209
	v_add_u32_e32 v235, s4, v210
	s_add_i32 s18, s15, 0x80
	v_mov_b64_e32 v[240:241], s[92:93]
	v_mov_b64_e32 v[242:243], s[94:95]

.LBB0_1598:
	ds_read_b128 v[36:39], v211 offset:12288
	ds_read_b128 v[52:55], v211 offset:12320
	ds_read_b128 v[56:59], v211 offset:18432
	ds_read_b128 v[60:63], v211 offset:18464
	v_exp_f32_e32 v84, v116
	v_exp_f32_e32 v98, v132
	s_waitcnt lgkmcnt(0)
	v_mfma_f32_32x32x16_bf16 v[36:51], v[36:39], v[168:171], 0
	v_exp_f32_e32 v85, v117
	v_exp_f32_e32 v116, v133
	v_exp_f32_e32 v117, v118
	v_exp_f32_e32 v118, v134
	v_exp_f32_e32 v125, v125
	v_exp_f32_e32 v132, v141
	v_exp_f32_e32 v129, v129
	v_mfma_f32_32x32x16_bf16 v[68:83], v[56:59], v[168:171], 0
	v_cvt_pk_bf16_f32 v84, v84, v85
	v_mfma_f32_32x32x16_bf16 v[36:51], v[52:55], v[148:151], v[36:51]
	ds_read_b128 v[52:55], v211 offset:12352
	ds_read_b128 v[56:59], v211 offset:12384
	v_mfma_f32_32x32x16_bf16 v[68:83], v[60:63], v[148:151], v[68:83]
	v_exp_f32_e32 v61, v126
	v_exp_f32_e32 v126, v142
	v_exp_f32_e32 v62, v127
	v_exp_f32_e32 v127, v143
	v_exp_f32_e32 v63, v128
	v_exp_f32_e32 v128, v144
	v_cvt_pk_bf16_f32 v61, v61, v62
	s_waitcnt lgkmcnt(0)
	v_mfma_f32_32x32x16_bf16 v[36:51], v[52:55], v[152:155], v[36:51]
	ds_read_b128 v[52:55], v211 offset:18496
	ds_read_b128 v[86:89], v211 offset:18528
	ds_read_b128 v[90:93], v226 offset:12288
	ds_read_b128 v[94:97], v226 offset:18432
	v_cvt_pk_bf16_f32 v62, v63, v129
	s_waitcnt lgkmcnt(0)
	v_mfma_f32_32x32x16_bf16 v[68:83], v[52:55], v[152:155], v[68:83]
	v_exp_f32_e32 v54, v145
	v_exp_f32_e32 v52, v130
	v_exp_f32_e32 v55, v146
	v_exp_f32_e32 v53, v131
	v_exp_f32_e32 v130, v147
	v_cvt_pk_bf16_f32 v54, v128, v54
	v_cvt_pk_bf16_f32 v63, v52, v53
	v_mfma_f32_32x32x16_bf16 v[36:51], v[56:59], v[156:159], v[36:51]
	ds_read_b128 v[56:59], v227 offset:12288
	ds_read_b128 v[236:239], v227 offset:18432
	v_cvt_pk_bf16_f32 v53, v126, v127
	v_cvt_pk_bf16_f32 v55, v55, v130
	v_mfma_f32_32x32x16_bf16 v[68:83], v[86:89], v[156:159], v[68:83]
	v_mfma_f32_32x32x16_bf16 v[36:51], v[90:93], v[160:163], v[36:51]
	v_exp_f32_e32 v90, v119
	v_exp_f32_e32 v91, v135
	v_exp_f32_e32 v92, v120
	v_exp_f32_e32 v93, v136
	v_exp_f32_e32 v119, v121
	v_exp_f32_e32 v120, v137
	v_exp_f32_e32 v121, v122
	v_mfma_f32_32x32x16_bf16 v[68:83], v[94:97], v[160:163], v[68:83]
	v_exp_f32_e32 v122, v139
	v_cvt_pk_bf16_f32 v85, v117, v90
	v_cvt_pk_bf16_f32 v86, v92, v119
	s_waitcnt lgkmcnt(0)
	v_mfma_f32_32x32x16_bf16 v[36:51], v[56:59], v[164:167], v[36:51]
	v_exp_f32_e32 v59, v138
	v_exp_f32_e32 v56, v123
	v_exp_f32_e32 v123, v124
	v_exp_f32_e32 v124, v140
	v_cvt_pk_bf16_f32 v57, v118, v91
	v_cvt_pk_bf16_f32 v87, v121, v56
	v_cvt_pk_bf16_f32 v56, v98, v116
	v_mfma_f32_32x32x16_bf16 v[68:83], v[236:239], v[164:167], v[68:83]
	v_cvt_pk_bf16_f32 v58, v93, v120
	v_cvt_pk_bf16_f32 v59, v59, v122
	v_cvt_pk_bf16_f32 v60, v123, v125
	v_cvt_pk_bf16_f32 v52, v124, v132
	v_max3_f32 v96, v36, v37, v68
	v_max_f32_e32 v97, v51, v51
	v_max3_f32 v96, v96, v69, v38
	ds_read_b64_tr_b16 v[120:121], v234 offset:0
	ds_read_b64_tr_b16 v[122:123], v234 offset:1024
	s_nop 0
	v_mfma_f32_32x32x16_bf16 v[100:115], v[240:243], v[84:87], v[100:115]
	v_max3_f32 v96, v96, v70, v71
	ds_read_b64_tr_b16 v[116:117], v235 offset:0
	ds_read_b64_tr_b16 v[118:119], v235 offset:1024
	ds_read_b64_tr_b16 v[92:93], v234 offset:2048
	ds_read_b64_tr_b16 v[94:95], v234 offset:3072
	ds_read_b64_tr_b16 v[88:89], v235 offset:2048
	s_nop 0
	v_max3_f32 v96, v96, v39, v40
	v_mfma_f32_32x32x16_bf16 v[100:115], v[240:243], v[60:63], v[100:115]
	v_max3_f32 v96, v96, v72, v73
	ds_read_b64_tr_b16 v[90:91], v235 offset:3072
	s_nop 0
	v_max3_f32 v96, v96, v41, v42
	v_max3_f32 v96, v96, v74, v75
	v_max3_f32 v96, v96, v43, v44
	v_mfma_f32_32x32x16_bf16 v[100:115], v[240:243], v[56:59], v[100:115]
	v_max3_f32 v96, v96, v76, v77
	v_max3_f32 v96, v96, v45, v46
	v_max3_f32 v96, v96, v78, v79
	v_max3_f32 v96, v96, v47, v48
	v_mfma_f32_32x32x16_bf16 v[100:115], v[240:243], v[52:55], v[100:115]
	v_max3_f32 v96, v96, v80, v81
	v_max3_f32 v96, v96, v49, v50
	v_max3_f32 v96, v96, v82, v83
	v_max_f32_e32 v96, v96, v96
	v_max_f32_e32 v96, v96, v97
	v_mov_b32_e32 v97, v96
	s_nop 1
	v_permlane32_swap_b32_e32 v96, v97
	v_sub_f32_e32 v96, v96, v66
	s_waitcnt lgkmcnt(0)
	s_nop 0
	v_mfma_f32_32x32x16_bf16 v[2:17], v[120:123], v[84:87], v[2:17]
	v_mfma_f32_32x32x16_bf16 v[18:33], v[116:119], v[84:87], v[18:33]
	v_mfma_f32_32x32x16_bf16 v[2:17], v[92:95], v[60:63], v[2:17]
	v_mfma_f32_32x32x16_bf16 v[18:33], v[88:91], v[60:63], v[18:33]
	ds_read_b64_tr_b16 v[60:61], v234 offset:4096
	ds_read_b64_tr_b16 v[62:63], v234 offset:5120
	ds_read_b64_tr_b16 v[84:85], v235 offset:4096
	ds_read_b64_tr_b16 v[86:87], v235 offset:5120
	ds_read_b64_tr_b16 v[88:89], v234 offset:6144
	ds_read_b64_tr_b16 v[90:91], v234 offset:7168
	ds_read_b64_tr_b16 v[92:93], v235 offset:6144
	ds_read_b64_tr_b16 v[94:95], v235 offset:7168
	s_nop 0
	s_waitcnt lgkmcnt(0)
	s_nop 0
	v_mfma_f32_32x32x16_bf16 v[2:17], v[60:63], v[56:59], v[2:17]
	v_mfma_f32_32x32x16_bf16 v[18:33], v[84:87], v[56:59], v[18:33]
	v_mfma_f32_32x32x16_bf16 v[2:17], v[88:91], v[52:55], v[2:17]
	v_mfma_f32_32x32x16_bf16 v[18:33], v[92:95], v[52:55], v[18:33]
	v_cmp_lt_f32_e32 vcc, s29, v96
	s_cbranch_vccz .LBB0_1600
	v_max_f32_e32 v52, v96, v96
	v_max_f32_e32 v53, 0, v52
	v_exp_f32_e64 v52, -v53
	v_add_f32_e32 v66, v66, v53
	v_mul_f32_e32 v34, v34, v52
	v_pk_mul_f32 v[114:115], v[114:115], v[52:53] op_sel_hi:[1,0]
	v_pk_mul_f32 v[112:113], v[112:113], v[52:53] op_sel_hi:[1,0]
	v_pk_mul_f32 v[110:111], v[110:111], v[52:53] op_sel_hi:[1,0]
	v_pk_mul_f32 v[108:109], v[108:109], v[52:53] op_sel_hi:[1,0]
	v_pk_mul_f32 v[106:107], v[106:107], v[52:53] op_sel_hi:[1,0]
	v_pk_mul_f32 v[104:105], v[104:105], v[52:53] op_sel_hi:[1,0]
	v_pk_mul_f32 v[102:103], v[102:103], v[52:53] op_sel_hi:[1,0]
	v_pk_mul_f32 v[100:101], v[100:101], v[52:53] op_sel_hi:[1,0]
	v_pk_mul_f32 v[32:33], v[52:53], v[32:33] op_sel_hi:[0,1]
	v_pk_mul_f32 v[30:31], v[52:53], v[30:31] op_sel_hi:[0,1]
	v_pk_mul_f32 v[28:29], v[52:53], v[28:29] op_sel_hi:[0,1]
	v_pk_mul_f32 v[26:27], v[52:53], v[26:27] op_sel_hi:[0,1]
	v_pk_mul_f32 v[24:25], v[52:53], v[24:25] op_sel_hi:[0,1]
	v_pk_mul_f32 v[22:23], v[52:53], v[22:23] op_sel_hi:[0,1]
	v_pk_mul_f32 v[20:21], v[52:53], v[20:21] op_sel_hi:[0,1]
	v_pk_mul_f32 v[18:19], v[52:53], v[18:19] op_sel_hi:[0,1]
	v_pk_mul_f32 v[16:17], v[52:53], v[16:17] op_sel_hi:[0,1]
	v_pk_mul_f32 v[14:15], v[52:53], v[14:15] op_sel_hi:[0,1]
	v_pk_mul_f32 v[12:13], v[52:53], v[12:13] op_sel_hi:[0,1]
	v_pk_mul_f32 v[10:11], v[52:53], v[10:11] op_sel_hi:[0,1]
	v_pk_mul_f32 v[8:9], v[52:53], v[8:9] op_sel_hi:[0,1]
	v_pk_mul_f32 v[6:7], v[52:53], v[6:7] op_sel_hi:[0,1]
	v_pk_mul_f32 v[4:5], v[52:53], v[4:5] op_sel_hi:[0,1]
	v_pk_mul_f32 v[2:3], v[52:53], v[2:3] op_sel_hi:[0,1]

.LBB0_1631:
	s_mov_b32 s31, s89
	ds_read_b128 v[52:55], v211
	ds_read_b128 v[56:59], v211 offset:32
	v_exp_f32_e32 v36, v36
	v_exp_f32_e32 v68, v68
	v_exp_f32_e32 v37, v37
	s_waitcnt lgkmcnt(0)
	v_mfma_f32_32x32x16_bf16 v[116:131], v[52:55], v[168:171], 0
	ds_read_b128 v[52:55], v211 offset:6144
	ds_read_b128 v[60:63], v211 offset:6176
	v_exp_f32_e32 v69, v69
	v_exp_f32_e32 v38, v38
	v_exp_f32_e32 v70, v70
	v_exp_f32_e32 v39, v39
	v_exp_f32_e32 v71, v71
	v_exp_f32_e32 v40, v40
	s_waitcnt lgkmcnt(0)
	v_mfma_f32_32x32x16_bf16 v[132:147], v[52:55], v[168:171], 0
	v_exp_f32_e32 v72, v72
	v_exp_f32_e32 v41, v41
	v_exp_f32_e32 v73, v73
	v_exp_f32_e32 v42, v42
	v_exp_f32_e32 v43, v43
	v_exp_f32_e32 v44, v44
	v_exp_f32_e32 v45, v45
	v_mfma_f32_32x32x16_bf16 v[116:131], v[56:59], v[148:151], v[116:131]
	ds_read_b128 v[52:55], v211 offset:64
	ds_read_b128 v[56:59], v211 offset:96
	v_exp_f32_e32 v46, v46
	v_exp_f32_e32 v47, v47
	v_cvt_pk_bf16_f32 v44, v44, v45
	v_cvt_pk_bf16_f32 v45, v46, v47
	v_mfma_f32_32x32x16_bf16 v[132:147], v[60:63], v[148:151], v[132:147]
	v_exp_f32_e32 v60, v78
	v_exp_f32_e32 v61, v79
	v_exp_f32_e32 v62, v48
	v_exp_f32_e32 v63, v80
	v_cvt_pk_bf16_f32 v48, v36, v37
	v_cvt_pk_bf16_f32 v37, v60, v61
	s_waitcnt lgkmcnt(0)
	v_mfma_f32_32x32x16_bf16 v[116:131], v[52:55], v[152:155], v[116:131]
	ds_read_b128 v[52:55], v211 offset:6208
	ds_read_b128 v[84:87], v211 offset:6240
	ds_read_b128 v[88:91], v226
	ds_read_b128 v[92:95], v226 offset:6144
	s_waitcnt lgkmcnt(0)
	v_mfma_f32_32x32x16_bf16 v[132:147], v[52:55], v[152:155], v[132:147]
	v_exp_f32_e32 v52, v81
	v_exp_f32_e32 v53, v50
	v_exp_f32_e32 v54, v82
	v_exp_f32_e32 v55, v51
	v_cvt_pk_bf16_f32 v50, v40, v41
	v_cvt_pk_bf16_f32 v51, v42, v43
	v_cvt_pk_bf16_f32 v40, v68, v69
	v_mfma_f32_32x32x16_bf16 v[116:131], v[56:59], v[156:159], v[116:131]
	ds_read_b128 v[56:59], v227
	ds_read_b128 v[236:239], v227 offset:6144
	v_cvt_pk_bf16_f32 v41, v70, v71
	v_cvt_pk_bf16_f32 v42, v72, v73
	v_cvt_pk_bf16_f32 v47, v53, v55
	v_mfma_f32_32x32x16_bf16 v[132:147], v[84:87], v[156:159], v[132:147]
	v_mfma_f32_32x32x16_bf16 v[116:131], v[88:91], v[160:163], v[116:131]
	v_mfma_f32_32x32x16_bf16 v[132:147], v[92:95], v[160:163], v[132:147]
	s_waitcnt lgkmcnt(0)
	v_mfma_f32_32x32x16_bf16 v[116:131], v[56:59], v[164:167], v[116:131]
	v_exp_f32_e32 v56, v74
	v_exp_f32_e32 v57, v75
	v_exp_f32_e32 v58, v76
	v_exp_f32_e32 v59, v77
	v_exp_f32_e32 v74, v49
	v_exp_f32_e32 v75, v83
	v_cvt_pk_bf16_f32 v49, v38, v39
	v_mfma_f32_32x32x16_bf16 v[132:147], v[236:239], v[164:167], v[132:147]
	v_cvt_pk_bf16_f32 v43, v56, v57
	v_cvt_pk_bf16_f32 v46, v62, v74
	v_cvt_pk_bf16_f32 v36, v58, v59
	v_cvt_pk_bf16_f32 v38, v63, v52
	v_cvt_pk_bf16_f32 v39, v54, v75
	v_max3_f32 v72, v116, v117, v132
	v_max_f32_e32 v73, v131, v131
	v_max3_f32 v72, v72, v133, v118
	ds_read_b64_tr_b16 v[68:69], v205 offset:0
	ds_read_b64_tr_b16 v[70:71], v205 offset:1024
	s_nop 0
	v_mfma_f32_32x32x16_bf16 v[100:115], v[240:243], v[48:51], v[100:115]
	v_max3_f32 v72, v72, v134, v135
	ds_read_b64_tr_b16 v[60:61], v67 offset:0
	ds_read_b64_tr_b16 v[62:63], v67 offset:1024
	ds_read_b64_tr_b16 v[56:57], v205 offset:2048
	ds_read_b64_tr_b16 v[58:59], v205 offset:3072
	ds_read_b64_tr_b16 v[52:53], v67 offset:2048
	s_nop 0
	v_max3_f32 v72, v72, v119, v120
	v_mfma_f32_32x32x16_bf16 v[100:115], v[240:243], v[44:47], v[100:115]
	v_max3_f32 v72, v72, v136, v137
	ds_read_b64_tr_b16 v[54:55], v67 offset:3072
	s_nop 0
	v_max3_f32 v72, v72, v121, v122
	v_max3_f32 v72, v72, v138, v139
	v_max3_f32 v72, v72, v123, v124
	v_mfma_f32_32x32x16_bf16 v[100:115], v[240:243], v[40:43], v[100:115]
	v_max3_f32 v72, v72, v140, v141
	v_max3_f32 v72, v72, v125, v126
	v_max3_f32 v72, v72, v142, v143
	v_max3_f32 v72, v72, v127, v128
	v_mfma_f32_32x32x16_bf16 v[100:115], v[240:243], v[36:39], v[100:115]
	v_max3_f32 v72, v72, v144, v145
	v_max3_f32 v72, v72, v129, v130
	v_max3_f32 v72, v72, v146, v147
	v_max_f32_e32 v72, v72, v72
	v_max_f32_e32 v72, v72, v73
	v_mov_b32_e32 v73, v72
	s_nop 1
	v_permlane32_swap_b32_e32 v72, v73
	v_sub_f32_e32 v72, v72, v66
	s_waitcnt lgkmcnt(0)
	s_nop 0
	v_mfma_f32_32x32x16_bf16 v[2:17], v[68:71], v[48:51], v[2:17]
	v_mfma_f32_32x32x16_bf16 v[18:33], v[60:63], v[48:51], v[18:33]
	v_mfma_f32_32x32x16_bf16 v[2:17], v[56:59], v[44:47], v[2:17]
	v_mfma_f32_32x32x16_bf16 v[18:33], v[52:55], v[44:47], v[18:33]
	ds_read_b64_tr_b16 v[44:45], v205 offset:4096
	ds_read_b64_tr_b16 v[46:47], v205 offset:5120
	ds_read_b64_tr_b16 v[48:49], v67 offset:4096
	ds_read_b64_tr_b16 v[50:51], v67 offset:5120
	ds_read_b64_tr_b16 v[52:53], v205 offset:6144
	ds_read_b64_tr_b16 v[54:55], v205 offset:7168
	ds_read_b64_tr_b16 v[56:57], v67 offset:6144
	ds_read_b64_tr_b16 v[58:59], v67 offset:7168
	s_nop 0
	s_waitcnt lgkmcnt(0)
	s_nop 0
	v_mfma_f32_32x32x16_bf16 v[2:17], v[44:47], v[40:43], v[2:17]
	v_mfma_f32_32x32x16_bf16 v[18:33], v[48:51], v[40:43], v[18:33]
	v_mfma_f32_32x32x16_bf16 v[2:17], v[52:55], v[36:39], v[2:17]
	v_mfma_f32_32x32x16_bf16 v[18:33], v[56:59], v[36:39], v[18:33]
	v_cmp_lt_f32_e32 vcc, s29, v72
	s_cbranch_vccz .LBB0_1633
	v_max_f32_e32 v36, v72, v72
	v_max_f32_e32 v37, 0, v36
	v_exp_f32_e64 v36, -v37
	v_add_f32_e32 v66, v66, v37
	v_mul_f32_e32 v34, v34, v36
	v_pk_mul_f32 v[114:115], v[114:115], v[36:37] op_sel_hi:[1,0]
	v_pk_mul_f32 v[112:113], v[112:113], v[36:37] op_sel_hi:[1,0]
	v_pk_mul_f32 v[110:111], v[110:111], v[36:37] op_sel_hi:[1,0]
	v_pk_mul_f32 v[108:109], v[108:109], v[36:37] op_sel_hi:[1,0]
	v_pk_mul_f32 v[106:107], v[106:107], v[36:37] op_sel_hi:[1,0]
	v_pk_mul_f32 v[104:105], v[104:105], v[36:37] op_sel_hi:[1,0]
	v_pk_mul_f32 v[102:103], v[102:103], v[36:37] op_sel_hi:[1,0]
	v_pk_mul_f32 v[100:101], v[100:101], v[36:37] op_sel_hi:[1,0]
	v_pk_mul_f32 v[32:33], v[36:37], v[32:33] op_sel_hi:[0,1]
	v_pk_mul_f32 v[30:31], v[36:37], v[30:31] op_sel_hi:[0,1]
	v_pk_mul_f32 v[28:29], v[36:37], v[28:29] op_sel_hi:[0,1]
	v_pk_mul_f32 v[26:27], v[36:37], v[26:27] op_sel_hi:[0,1]
	v_pk_mul_f32 v[24:25], v[36:37], v[24:25] op_sel_hi:[0,1]
	v_pk_mul_f32 v[22:23], v[36:37], v[22:23] op_sel_hi:[0,1]
	v_pk_mul_f32 v[20:21], v[36:37], v[20:21] op_sel_hi:[0,1]
	v_pk_mul_f32 v[18:19], v[36:37], v[18:19] op_sel_hi:[0,1]
	v_pk_mul_f32 v[16:17], v[36:37], v[16:17] op_sel_hi:[0,1]
	v_pk_mul_f32 v[14:15], v[36:37], v[14:15] op_sel_hi:[0,1]
	v_pk_mul_f32 v[12:13], v[36:37], v[12:13] op_sel_hi:[0,1]
	v_pk_mul_f32 v[10:11], v[36:37], v[10:11] op_sel_hi:[0,1]
	v_pk_mul_f32 v[8:9], v[36:37], v[8:9] op_sel_hi:[0,1]
	v_pk_mul_f32 v[6:7], v[36:37], v[6:7] op_sel_hi:[0,1]
	v_pk_mul_f32 v[4:5], v[36:37], v[4:5] op_sel_hi:[0,1]
	v_pk_mul_f32 v[2:3], v[36:37], v[2:3] op_sel_hi:[0,1]

.LBB0_1983:
	v_and_or_b32 v89, v189, 3, v187
	v_lshlrev_b32_e32 v89, 7, v89
	v_lshlrev_b32_e32 v87, 5, v87
	v_and_b32_e32 v88, 24, v88
	s_waitcnt lgkmcnt(0)
	s_barrier
	v_or3_b32 v87, v89, v87, v88
	v_lshlrev_b32_e32 v86, 6, v86
	v_and_or_b32 v177, v86, 64, v87
	v_bitop3_b32 v178, v87, 64, v86 bitop3:0x34
	s_cmp_lt_i32 s85, 3
	s_cbranch_scc1 .LBB0_2059
	v_mov_b32_e32 v149, v99
	v_ashrrev_i32_e32 v86, 6, v185
	v_and_b32_e32 v87, 7, v185
	v_lshl_add_u64 v[154:155], s[18:19], 0, v[148:149]
	v_and_b32_e32 v149, -2, v86
	v_and_b32_e32 v86, 30, v189
	v_lshl_add_u32 v88, v87, 10, 0
	v_lshlrev_b32_e32 v87, 4, v87
	v_lshl_or_b32 v156, v86, 11, v87
	v_lshlrev_b32_e32 v86, 3, v179
	v_and_b32_e32 v87, 4, v185
	v_and_or_b32 v86, v86, 24, v87
	v_lshlrev_b32_e32 v158, 2, v86
	v_bitop3_b32 v86, v185, 5, 7 bitop3:0x6c
	v_lshlrev_b32_e32 v87, 3, v86
	v_bitop3_b32 v86, v87, 28, v86 bitop3:0xc8
	v_lshlrev_b32_e32 v168, 2, v86
	v_bitop3_b32 v86, v185, 6, 7 bitop3:0x6c
	v_lshlrev_b32_e32 v87, 3, v86
	v_bitop3_b32 v86, v87, 28, v86 bitop3:0xc8
	v_lshlrev_b32_e32 v170, 2, v86
	v_bitop3_b32 v86, v185, 7, v185 bitop3:0xc
	v_bfe_u32 v89, v189, 2, 3
	v_lshlrev_b32_e32 v87, 3, v86
	s_add_i32 s4, 0, 0x4000
	v_bitop3_b32 v89, v89, v185, 7 bitop3:0x78
	v_lshlrev_b32_e32 v90, 2, v189
	v_bitop3_b32 v86, v87, 28, v86 bitop3:0xc8
	v_add_u32_e32 v200, s4, v177
	v_add_u32_e32 v201, s4, v178
	s_add_i32 s4, 0, 0x6000
	v_lshlrev_b32_e32 v89, 4, v89
	v_and_b32_e32 v90, 8, v90
	v_lshlrev_b32_e32 v172, 2, v86
	v_add_u32_e32 v202, s4, v177
	v_add_u32_e32 v203, s4, v178
	v_add_u32_e32 v86, s86, v187
	s_sub_i32 s4, s89, s86
	s_lshl_b32 s97, s90, 4
	s_lshl_b32 s2, s90, 11
	v_add3_u32 v198, v88, v89, v90
	v_mov_b32_e32 v157, v99
	s_lshl_b32 s3, s91, 1
	v_and_b32_e32 v199, 28, v186
	s_mov_b32 s76, 3
	v_mov_b32_e32 v159, v99
	v_xor_b32_e32 v160, 32, v158
	v_mov_b32_e32 v161, v99
	v_xor_b32_e32 v162, 64, v158
	v_mov_b32_e32 v163, v99
	v_xor_b32_e32 v164, 0x60, v158
	v_mov_b32_e32 v165, v99
	v_xor_b32_e32 v166, 16, v158
	v_mov_b32_e32 v167, v99
	v_mov_b32_e32 v169, v99
	v_mov_b32_e32 v171, v99
	v_mov_b32_e32 v173, v99
	s_mov_b32 s14, 0
	v_cmp_eq_u32_e64 s[36:37], 0, v179
	v_mov_b32_e32 v151, v99
	v_mov_b32_e32 v153, v99
	s_sub_i32 s56, s86, s89
	v_sub_u32_e32 v204, v86, v176
	s_add_i32 s6, s4, 0xffffff9f
	v_mov_b64_e32 v[240:241], s[92:93]
	v_mov_b64_e32 v[242:243], s[94:95]

.LBB0_2006:
	v_max3_f32 v86, v100, v101, v116
	v_max_f32_e32 v87, v115, v115
	v_max3_f32 v86, v86, v117, v102
	s_nop 0
	v_mfma_f32_32x32x16_bf16 v[34:49], v[240:243], v[58:61], v[34:49]
	v_max3_f32 v86, v86, v118, v119
	v_max3_f32 v86, v86, v103, v104
	v_max3_f32 v86, v86, v120, v121
	v_max3_f32 v86, v86, v105, v106
	v_mfma_f32_32x32x16_bf16 v[34:49], v[240:243], v[62:65], v[34:49]
	v_max3_f32 v86, v86, v122, v123
	v_max3_f32 v86, v86, v107, v108
	v_max3_f32 v86, v86, v124, v125
	v_max3_f32 v86, v86, v109, v110
	v_mfma_f32_32x32x16_bf16 v[34:49], v[240:243], v[54:57], v[34:49]
	v_max3_f32 v86, v86, v126, v127
	v_max3_f32 v86, v86, v111, v112
	v_max3_f32 v86, v86, v128, v129
	v_max3_f32 v86, v86, v113, v114
	v_mfma_f32_32x32x16_bf16 v[34:49], v[240:243], v[50:53], v[34:49]
	v_max3_f32 v86, v86, v130, v131
	v_max_f32_e32 v86, v86, v86
	v_max_f32_e32 v86, v86, v87
	v_mov_b32_e32 v87, v86
	s_nop 1
	v_permlane32_swap_b32_e32 v86, v87
	v_sub_f32_e32 v86, v86, v184
	s_waitcnt lgkmcnt(0)
	s_nop 0
	v_mfma_f32_32x32x16_bf16 v[18:33], v[78:81], v[58:61], v[18:33]
	v_mfma_f32_32x32x16_bf16 v[2:17], v[74:77], v[58:61], v[2:17]
	ds_read_b64_tr_b16 v[58:59], v200 offset:4096
	ds_read_b64_tr_b16 v[60:61], v200 offset:5120
	v_mfma_f32_32x32x16_bf16 v[18:33], v[70:73], v[62:65], v[18:33]
	v_mfma_f32_32x32x16_bf16 v[2:17], v[66:69], v[62:65], v[2:17]
	ds_read_b64_tr_b16 v[62:63], v201 offset:4096
	ds_read_b64_tr_b16 v[64:65], v201 offset:5120
	ds_read_b64_tr_b16 v[66:67], v200 offset:6144
	ds_read_b64_tr_b16 v[68:69], v200 offset:7168
	ds_read_b64_tr_b16 v[70:71], v201 offset:6144
	ds_read_b64_tr_b16 v[72:73], v201 offset:7168
	s_nop 0
	s_waitcnt lgkmcnt(0)
	s_nop 0
	v_mfma_f32_32x32x16_bf16 v[18:33], v[58:61], v[54:57], v[18:33]
	v_mfma_f32_32x32x16_bf16 v[2:17], v[62:65], v[54:57], v[2:17]
	v_mfma_f32_32x32x16_bf16 v[18:33], v[66:69], v[50:53], v[18:33]
	v_mfma_f32_32x32x16_bf16 v[2:17], v[70:73], v[50:53], v[2:17]
	v_cmp_lt_f32_e32 vcc, s29, v86
	s_cbranch_vccz .LBB0_2008
	v_max_f32_e32 v50, v86, v86
	v_max_f32_e32 v51, 0, v50
	v_exp_f32_e64 v50, -v51
	v_add_f32_e32 v184, v184, v51
	v_mul_f32_e32 v175, v175, v50
	v_pk_mul_f32 v[48:49], v[48:49], v[50:51] op_sel_hi:[1,0]
	v_pk_mul_f32 v[46:47], v[46:47], v[50:51] op_sel_hi:[1,0]
	v_pk_mul_f32 v[44:45], v[44:45], v[50:51] op_sel_hi:[1,0]
	v_pk_mul_f32 v[42:43], v[42:43], v[50:51] op_sel_hi:[1,0]
	v_pk_mul_f32 v[40:41], v[40:41], v[50:51] op_sel_hi:[1,0]
	v_pk_mul_f32 v[38:39], v[38:39], v[50:51] op_sel_hi:[1,0]
	v_pk_mul_f32 v[36:37], v[36:37], v[50:51] op_sel_hi:[1,0]
	v_pk_mul_f32 v[34:35], v[34:35], v[50:51] op_sel_hi:[1,0]
	v_pk_mul_f32 v[16:17], v[50:51], v[16:17] op_sel_hi:[0,1]
	v_pk_mul_f32 v[14:15], v[50:51], v[14:15] op_sel_hi:[0,1]
	v_pk_mul_f32 v[12:13], v[50:51], v[12:13] op_sel_hi:[0,1]
	v_pk_mul_f32 v[10:11], v[50:51], v[10:11] op_sel_hi:[0,1]
	v_pk_mul_f32 v[8:9], v[50:51], v[8:9] op_sel_hi:[0,1]
	v_pk_mul_f32 v[6:7], v[50:51], v[6:7] op_sel_hi:[0,1]
	v_pk_mul_f32 v[4:5], v[50:51], v[4:5] op_sel_hi:[0,1]
	v_pk_mul_f32 v[2:3], v[50:51], v[2:3] op_sel_hi:[0,1]
	v_pk_mul_f32 v[32:33], v[50:51], v[32:33] op_sel_hi:[0,1]
	v_pk_mul_f32 v[30:31], v[50:51], v[30:31] op_sel_hi:[0,1]
	v_pk_mul_f32 v[28:29], v[50:51], v[28:29] op_sel_hi:[0,1]
	v_pk_mul_f32 v[26:27], v[50:51], v[26:27] op_sel_hi:[0,1]
	v_pk_mul_f32 v[24:25], v[50:51], v[24:25] op_sel_hi:[0,1]
	v_pk_mul_f32 v[22:23], v[50:51], v[22:23] op_sel_hi:[0,1]
	v_pk_mul_f32 v[20:21], v[50:51], v[20:21] op_sel_hi:[0,1]
	v_pk_mul_f32 v[18:19], v[50:51], v[18:19] op_sel_hi:[0,1]

.LBB0_2044:
	v_max3_f32 v98, v50, v51, v66
	v_max_f32_e32 v120, v65, v65
	v_max3_f32 v98, v98, v67, v52
	s_nop 0
	v_mfma_f32_32x32x16_bf16 v[34:49], v[240:243], v[94:97], v[34:49]
	v_max3_f32 v98, v98, v68, v69
	v_max3_f32 v98, v98, v53, v54
	v_max3_f32 v98, v98, v70, v71
	v_max3_f32 v98, v98, v55, v56
	v_mfma_f32_32x32x16_bf16 v[34:49], v[240:243], v[100:103], v[34:49]
	v_max3_f32 v98, v98, v72, v73
	v_max3_f32 v98, v98, v57, v58
	v_max3_f32 v98, v98, v74, v75
	v_max3_f32 v98, v98, v59, v60
	v_mfma_f32_32x32x16_bf16 v[34:49], v[240:243], v[90:93], v[34:49]
	v_max3_f32 v98, v98, v76, v77
	v_max3_f32 v98, v98, v61, v62
	v_max3_f32 v98, v98, v78, v79
	v_max3_f32 v98, v98, v63, v64
	v_mfma_f32_32x32x16_bf16 v[34:49], v[240:243], v[86:89], v[34:49]
	v_max3_f32 v98, v98, v80, v81
	v_max_f32_e32 v98, v98, v98
	v_max_f32_e32 v98, v98, v120
	v_mov_b32_e32 v120, v98
	s_nop 1
	v_permlane32_swap_b32_e32 v98, v120
	v_sub_f32_e32 v120, v98, v184
	s_waitcnt lgkmcnt(0)
	s_nop 0
	v_mfma_f32_32x32x16_bf16 v[18:33], v[116:119], v[94:97], v[18:33]
	v_mfma_f32_32x32x16_bf16 v[2:17], v[112:115], v[94:97], v[2:17]
	ds_read_b64_tr_b16 v[94:95], v202 offset:4096
	ds_read_b64_tr_b16 v[96:97], v202 offset:5120
	v_mfma_f32_32x32x16_bf16 v[18:33], v[108:111], v[100:103], v[18:33]
	v_mfma_f32_32x32x16_bf16 v[2:17], v[104:107], v[100:103], v[2:17]
	ds_read_b64_tr_b16 v[100:101], v203 offset:4096
	ds_read_b64_tr_b16 v[102:103], v203 offset:5120
	ds_read_b64_tr_b16 v[104:105], v202 offset:6144
	ds_read_b64_tr_b16 v[106:107], v202 offset:7168
	ds_read_b64_tr_b16 v[108:109], v203 offset:6144
	ds_read_b64_tr_b16 v[110:111], v203 offset:7168
	s_nop 0
	s_waitcnt lgkmcnt(0)
	s_nop 0
	v_mfma_f32_32x32x16_bf16 v[18:33], v[94:97], v[90:93], v[18:33]
	v_mfma_f32_32x32x16_bf16 v[2:17], v[100:103], v[90:93], v[2:17]
	v_mfma_f32_32x32x16_bf16 v[18:33], v[104:107], v[86:89], v[18:33]
	v_mfma_f32_32x32x16_bf16 v[2:17], v[108:111], v[86:89], v[2:17]
	v_cmp_lt_f32_e32 vcc, s29, v120
	s_cbranch_vccz .LBB0_2046
	v_max_f32_e32 v86, v120, v120
	v_max_f32_e32 v87, 0, v86
	v_exp_f32_e64 v86, -v87
	v_add_f32_e32 v184, v184, v87
	v_mul_f32_e32 v175, v175, v86
	v_pk_mul_f32 v[48:49], v[48:49], v[86:87] op_sel_hi:[1,0]
	v_pk_mul_f32 v[46:47], v[46:47], v[86:87] op_sel_hi:[1,0]
	v_pk_mul_f32 v[44:45], v[44:45], v[86:87] op_sel_hi:[1,0]
	v_pk_mul_f32 v[42:43], v[42:43], v[86:87] op_sel_hi:[1,0]
	v_pk_mul_f32 v[40:41], v[40:41], v[86:87] op_sel_hi:[1,0]
	v_pk_mul_f32 v[38:39], v[38:39], v[86:87] op_sel_hi:[1,0]
	v_pk_mul_f32 v[36:37], v[36:37], v[86:87] op_sel_hi:[1,0]
	v_pk_mul_f32 v[34:35], v[34:35], v[86:87] op_sel_hi:[1,0]
	v_pk_mul_f32 v[16:17], v[86:87], v[16:17] op_sel_hi:[0,1]
	v_pk_mul_f32 v[14:15], v[86:87], v[14:15] op_sel_hi:[0,1]
	v_pk_mul_f32 v[12:13], v[86:87], v[12:13] op_sel_hi:[0,1]
	v_pk_mul_f32 v[10:11], v[86:87], v[10:11] op_sel_hi:[0,1]
	v_pk_mul_f32 v[8:9], v[86:87], v[8:9] op_sel_hi:[0,1]
	v_pk_mul_f32 v[6:7], v[86:87], v[6:7] op_sel_hi:[0,1]
	v_pk_mul_f32 v[4:5], v[86:87], v[4:5] op_sel_hi:[0,1]
	v_pk_mul_f32 v[2:3], v[86:87], v[2:3] op_sel_hi:[0,1]
	v_pk_mul_f32 v[32:33], v[86:87], v[32:33] op_sel_hi:[0,1]
	v_pk_mul_f32 v[30:31], v[86:87], v[30:31] op_sel_hi:[0,1]
	v_pk_mul_f32 v[28:29], v[86:87], v[28:29] op_sel_hi:[0,1]
	v_pk_mul_f32 v[26:27], v[86:87], v[26:27] op_sel_hi:[0,1]
	v_pk_mul_f32 v[24:25], v[86:87], v[24:25] op_sel_hi:[0,1]
	v_pk_mul_f32 v[22:23], v[86:87], v[22:23] op_sel_hi:[0,1]
	v_pk_mul_f32 v[20:21], v[86:87], v[20:21] op_sel_hi:[0,1]
	v_pk_mul_f32 v[18:19], v[86:87], v[18:19] op_sel_hi:[0,1]
